# index score loop: iq B fragments of k-steps 0 and 2 of the next head prefetched from LDS during the current head (2 alternating slot pairs in v240-255), k-step 3 read right after k-step 1's MFMA, coun
# baseline (speedup 1.0000x reference)
.LBB0_409:
	v_cndmask_b32_e64 v2, 0, 1, s[0:1]
	v_cmp_ne_u32_e32 vcc, 1, v2
	v_or_b32_e32 v2, s8, v168
	v_lshlrev_b32_e32 v2, 9, v2
	v_or_b32_e32 v169, s8, v1
	v_lshl_add_u64 v[4:5], v[2:3], 2, s[2:3]
	v_mad_u32_u24 v170, v169, s91, v135
	global_load_dwordx4 v[36:39], v[4:5], off offset:336
	global_load_dwordx4 v[40:43], v[4:5], off offset:320
	ds_read_b128 v[4:7], v170
	ds_read_b128 v[52:55], v170 offset:32
	s_waitcnt lgkmcnt(1)
	v_mfma_f32_32x32x16_bf16 v[4:19], v[20:23], v[4:7], 0
	s_mov_b32 s8, 32
	s_mov_b64 s[0:1], 0
	s_and_b64 vcc, exec, vcc
	ds_read_b128 v[68:71], v170 offset:160
	ds_read_b128 v[84:87], v170 offset:288
	ds_read_b128 v[102:105], v170 offset:416
	ds_read_b128 v[118:121], v170 offset:544
	s_waitcnt lgkmcnt(4)
	v_mfma_f32_32x32x16_bf16 v[4:19], v[24:27], v[52:55], v[4:19]
	ds_read_b128 v[52:55], v170 offset:64
	ds_read_b128 v[136:139], v170 offset:672
	ds_read_b128 v[152:155], v170 offset:800
	ds_read_b128 v[172:175], v170 offset:928
	s_waitcnt vmcnt(1)
	v_mul_f32_e32 v36, 0x3d3504f3, v36
	s_waitcnt lgkmcnt(3)
	v_mfma_f32_32x32x16_bf16 v[4:19], v[28:31], v[52:55], v[4:19]
	ds_read_b128 v[52:55], v170 offset:96
	ds_read_b128 v[240:243], v170 offset:128
	ds_read_b128 v[248:251], v170 offset:192
	s_waitcnt vmcnt(0)
	v_mul_f32_e32 v2, 0x3d3504f3, v40
	v_mul_f32_e32 v40, 0x3d3504f3, v41
	v_mul_f32_e32 v42, 0x3d3504f3, v42
	v_mul_f32_e32 v100, 0x3d3504f3, v43
	v_mul_f32_e32 v134, 0x3d3504f3, v37
	v_mul_f32_e32 v38, 0x3d3504f3, v38
	s_waitcnt lgkmcnt(2)
	v_mfma_f32_32x32x16_bf16 v[4:19], v[32:35], v[52:55], v[4:19]
	s_nop 11
	v_max_f32_e32 v66, 0, v4
	v_max_f32_e32 v67, 0, v5
	v_max_f32_e32 v64, 0, v6
	v_max_f32_e32 v65, 0, v7
	v_max_f32_e32 v62, 0, v8
	v_max_f32_e32 v63, 0, v9
	v_max_f32_e32 v60, 0, v10
	v_max_f32_e32 v61, 0, v11
	v_max_f32_e32 v58, 0, v12
	v_max_f32_e32 v59, 0, v13
	v_max_f32_e32 v56, 0, v14
	v_max_f32_e32 v57, 0, v15
	v_max_f32_e32 v54, 0, v16
	v_max_f32_e32 v55, 0, v17
	v_max_f32_e32 v52, 0, v18
	v_max_f32_e32 v53, 0, v19
	ds_read_b128 v[244:247], v170 offset:256
	ds_read_b128 v[252:255], v170 offset:320
	s_waitcnt lgkmcnt(3)
	v_mfma_f32_32x32x16_bf16 v[4:19], v[20:23], v[240:243], 0
	v_fma_f32 v66, v2, v66, 0
	v_fma_f32 v67, v2, v67, 0
	v_fma_f32 v64, v2, v64, 0
	v_fma_f32 v65, v2, v65, 0
	v_fma_f32 v62, v2, v62, 0
	v_fma_f32 v63, v2, v63, 0
	v_pk_fma_f32 v[60:61], v[2:3], v[60:61], 0 op_sel_hi:[0,1,0]
	v_pk_fma_f32 v[58:59], v[2:3], v[58:59], 0 op_sel_hi:[0,1,0]
	v_pk_fma_f32 v[56:57], v[2:3], v[56:57], 0 op_sel_hi:[0,1,0]
	v_pk_fma_f32 v[54:55], v[2:3], v[54:55], 0 op_sel_hi:[0,1,0]
	v_mfma_f32_32x32x16_bf16 v[4:19], v[24:27], v[68:71], v[4:19]
	ds_read_b128 v[68:71], v170 offset:224
	v_fma_f32 v52, v2, v52, 0
	v_fma_f32 v53, v2, v53, 0
	v_mul_u32_u24_e32 v2, s37, v169
	s_waitcnt lgkmcnt(3)
	v_mfma_f32_32x32x16_bf16 v[4:19], v[28:31], v[248:251], v[4:19]
	s_waitcnt lgkmcnt(0)
	v_mfma_f32_32x32x16_bf16 v[4:19], v[32:35], v[68:71], v[4:19]
	s_nop 11
	v_max_f32_e32 v82, 0, v4
	v_max_f32_e32 v83, 0, v5
	v_max_f32_e32 v80, 0, v6
	v_max_f32_e32 v81, 0, v7
	v_max_f32_e32 v78, 0, v8
	v_max_f32_e32 v79, 0, v9
	v_max_f32_e32 v76, 0, v10
	v_max_f32_e32 v77, 0, v11
	v_max_f32_e32 v74, 0, v12
	v_max_f32_e32 v75, 0, v13
	v_max_f32_e32 v72, 0, v14
	v_max_f32_e32 v73, 0, v15
	v_max_f32_e32 v70, 0, v16
	v_max_f32_e32 v71, 0, v17
	v_max_f32_e32 v68, 0, v18
	v_max_f32_e32 v69, 0, v19
	ds_read_b128 v[240:243], v170 offset:384
	ds_read_b128 v[248:251], v170 offset:448
	s_waitcnt lgkmcnt(2)
	v_mfma_f32_32x32x16_bf16 v[4:19], v[20:23], v[244:247], 0
	v_fma_f32 v66, v40, v82, v66
	v_fma_f32 v67, v40, v83, v67
	v_fma_f32 v64, v40, v80, v64
	v_fma_f32 v65, v40, v81, v65
	v_fma_f32 v62, v40, v78, v62
	v_fma_f32 v63, v40, v79, v63
	v_pk_fma_f32 v[60:61], v[40:41], v[76:77], v[60:61] op_sel_hi:[0,1,1]
	v_pk_fma_f32 v[58:59], v[40:41], v[74:75], v[58:59] op_sel_hi:[0,1,1]
	v_pk_fma_f32 v[56:57], v[40:41], v[72:73], v[56:57] op_sel_hi:[0,1,1]
	v_pk_fma_f32 v[54:55], v[40:41], v[70:71], v[54:55] op_sel_hi:[0,1,1]
	v_mfma_f32_32x32x16_bf16 v[4:19], v[24:27], v[84:87], v[4:19]
	ds_read_b128 v[84:87], v170 offset:352
	v_pk_fma_f32 v[40:41], v[40:41], v[68:69], v[52:53] op_sel_hi:[0,1,1]
	s_waitcnt lgkmcnt(3)
	v_mfma_f32_32x32x16_bf16 v[4:19], v[28:31], v[252:255], v[4:19]
	s_waitcnt lgkmcnt(0)
	v_mfma_f32_32x32x16_bf16 v[4:19], v[32:35], v[84:87], v[4:19]
	s_nop 11
	v_max_f32_e32 v98, 0, v4
	v_max_f32_e32 v99, 0, v5
	v_max_f32_e32 v96, 0, v6
	v_max_f32_e32 v97, 0, v7
	v_max_f32_e32 v94, 0, v8
	v_max_f32_e32 v95, 0, v9
	v_max_f32_e32 v92, 0, v10
	v_max_f32_e32 v93, 0, v11
	v_max_f32_e32 v90, 0, v12
	v_max_f32_e32 v91, 0, v13
	v_max_f32_e32 v88, 0, v14
	v_max_f32_e32 v89, 0, v15
	v_max_f32_e32 v86, 0, v16
	v_max_f32_e32 v87, 0, v17
	v_max_f32_e32 v84, 0, v18
	v_max_f32_e32 v85, 0, v19
	ds_read_b128 v[244:247], v170 offset:512
	ds_read_b128 v[252:255], v170 offset:576
	s_waitcnt lgkmcnt(2)
	v_mfma_f32_32x32x16_bf16 v[4:19], v[20:23], v[240:243], 0
	v_fma_f32 v66, v42, v98, v66
	v_fma_f32 v67, v42, v99, v67
	v_fma_f32 v64, v42, v96, v64
	v_fma_f32 v65, v42, v97, v65
	v_fma_f32 v62, v42, v94, v62
	v_fma_f32 v63, v42, v95, v63
	v_pk_fma_f32 v[60:61], v[42:43], v[92:93], v[60:61] op_sel_hi:[0,1,1]
	v_pk_fma_f32 v[58:59], v[42:43], v[90:91], v[58:59] op_sel_hi:[0,1,1]
	v_pk_fma_f32 v[56:57], v[42:43], v[88:89], v[56:57] op_sel_hi:[0,1,1]
	v_pk_fma_f32 v[54:55], v[42:43], v[86:87], v[54:55] op_sel_hi:[0,1,1]
	v_mfma_f32_32x32x16_bf16 v[4:19], v[24:27], v[102:105], v[4:19]
	ds_read_b128 v[102:105], v170 offset:480
	v_fma_f32 v40, v42, v84, v40
	v_fma_f32 v41, v42, v85, v41
	s_waitcnt lgkmcnt(3)
	v_mfma_f32_32x32x16_bf16 v[4:19], v[28:31], v[248:251], v[4:19]
	s_waitcnt lgkmcnt(0)
	v_mfma_f32_32x32x16_bf16 v[4:19], v[32:35], v[102:105], v[4:19]
	s_nop 11
	v_max_f32_e32 v116, 0, v4
	v_max_f32_e32 v117, 0, v5
	v_max_f32_e32 v114, 0, v6
	v_max_f32_e32 v115, 0, v7
	v_max_f32_e32 v112, 0, v8
	v_max_f32_e32 v113, 0, v9
	v_max_f32_e32 v110, 0, v10
	v_max_f32_e32 v111, 0, v11
	v_max_f32_e32 v108, 0, v12
	v_max_f32_e32 v109, 0, v13
	v_max_f32_e32 v106, 0, v14
	v_max_f32_e32 v107, 0, v15
	v_max_f32_e32 v104, 0, v16
	v_max_f32_e32 v105, 0, v17
	v_max_f32_e32 v102, 0, v18
	v_max_f32_e32 v103, 0, v19
	ds_read_b128 v[240:243], v170 offset:640
	ds_read_b128 v[248:251], v170 offset:704
	s_waitcnt lgkmcnt(2)
	v_mfma_f32_32x32x16_bf16 v[4:19], v[20:23], v[244:247], 0
	v_fma_f32 v66, v100, v116, v66
	v_fma_f32 v67, v100, v117, v67
	v_fma_f32 v64, v100, v114, v64
	v_fma_f32 v65, v100, v115, v65
	v_fma_f32 v62, v100, v112, v62
	v_fma_f32 v63, v100, v113, v63
	v_pk_fma_f32 v[60:61], v[100:101], v[110:111], v[60:61] op_sel_hi:[0,1,1]
	v_pk_fma_f32 v[58:59], v[100:101], v[108:109], v[58:59] op_sel_hi:[0,1,1]
	v_pk_fma_f32 v[56:57], v[100:101], v[106:107], v[56:57] op_sel_hi:[0,1,1]
	v_pk_fma_f32 v[54:55], v[100:101], v[104:105], v[54:55] op_sel_hi:[0,1,1]
	v_mfma_f32_32x32x16_bf16 v[4:19], v[24:27], v[118:121], v[4:19]
	ds_read_b128 v[118:121], v170 offset:608
	v_fma_f32 v40, v100, v102, v40
	v_fma_f32 v41, v100, v103, v41
	s_waitcnt lgkmcnt(3)
	v_mfma_f32_32x32x16_bf16 v[4:19], v[28:31], v[252:255], v[4:19]
	s_waitcnt lgkmcnt(0)
	v_mfma_f32_32x32x16_bf16 v[4:19], v[32:35], v[118:121], v[4:19]
	s_nop 11
	v_max_f32_e32 v132, 0, v4
	v_max_f32_e32 v133, 0, v5
	v_max_f32_e32 v130, 0, v6
	v_max_f32_e32 v131, 0, v7
	v_max_f32_e32 v128, 0, v8
	v_max_f32_e32 v129, 0, v9
	v_max_f32_e32 v126, 0, v10
	v_max_f32_e32 v127, 0, v11
	v_max_f32_e32 v124, 0, v12
	v_max_f32_e32 v125, 0, v13
	v_max_f32_e32 v122, 0, v14
	v_max_f32_e32 v123, 0, v15
	v_max_f32_e32 v120, 0, v16
	v_max_f32_e32 v121, 0, v17
	v_max_f32_e32 v118, 0, v18
	v_max_f32_e32 v119, 0, v19
	ds_read_b128 v[244:247], v170 offset:768
	ds_read_b128 v[252:255], v170 offset:832
	s_waitcnt lgkmcnt(2)
	v_mfma_f32_32x32x16_bf16 v[4:19], v[20:23], v[240:243], 0
	v_fma_f32 v66, v36, v132, v66
	v_fma_f32 v67, v36, v133, v67
	v_fma_f32 v64, v36, v130, v64
	v_fma_f32 v65, v36, v131, v65
	v_fma_f32 v62, v36, v128, v62
	v_fma_f32 v63, v36, v129, v63
	v_pk_fma_f32 v[60:61], v[36:37], v[126:127], v[60:61] op_sel_hi:[0,1,1]
	v_pk_fma_f32 v[58:59], v[36:37], v[124:125], v[58:59] op_sel_hi:[0,1,1]
	v_pk_fma_f32 v[56:57], v[36:37], v[122:123], v[56:57] op_sel_hi:[0,1,1]
	v_pk_fma_f32 v[54:55], v[36:37], v[120:121], v[54:55] op_sel_hi:[0,1,1]
	v_mfma_f32_32x32x16_bf16 v[4:19], v[24:27], v[136:139], v[4:19]
	ds_read_b128 v[136:139], v170 offset:736
	v_pk_fma_f32 v[36:37], v[36:37], v[118:119], v[40:41] op_sel_hi:[0,1,1]
	s_waitcnt lgkmcnt(3)
	v_mfma_f32_32x32x16_bf16 v[4:19], v[28:31], v[248:251], v[4:19]
	s_waitcnt lgkmcnt(0)
	v_mfma_f32_32x32x16_bf16 v[4:19], v[32:35], v[136:139], v[4:19]
	s_nop 11
	v_max_f32_e32 v150, 0, v4
	v_max_f32_e32 v151, 0, v5
	v_max_f32_e32 v148, 0, v6
	v_max_f32_e32 v149, 0, v7
	v_max_f32_e32 v146, 0, v8
	v_max_f32_e32 v147, 0, v9
	v_max_f32_e32 v144, 0, v10
	v_max_f32_e32 v145, 0, v11
	v_max_f32_e32 v142, 0, v12
	v_max_f32_e32 v143, 0, v13
	v_max_f32_e32 v140, 0, v14
	v_max_f32_e32 v141, 0, v15
	v_max_f32_e32 v138, 0, v16
	v_max_f32_e32 v139, 0, v17
	v_max_f32_e32 v136, 0, v18
	v_max_f32_e32 v137, 0, v19
	ds_read_b128 v[240:243], v170 offset:896
	ds_read_b128 v[248:251], v170 offset:960
	s_waitcnt lgkmcnt(2)
	v_mfma_f32_32x32x16_bf16 v[4:19], v[20:23], v[244:247], 0
	v_fma_f32 v66, v134, v150, v66
	v_fma_f32 v67, v134, v151, v67
	v_fma_f32 v64, v134, v148, v64
	v_fma_f32 v65, v134, v149, v65
	v_fma_f32 v36, v134, v136, v36
	v_fma_f32 v37, v134, v137, v37
	v_pk_fma_f32 v[62:63], v[134:135], v[146:147], v[62:63] op_sel_hi:[0,1,1]
	v_pk_fma_f32 v[60:61], v[134:135], v[144:145], v[60:61] op_sel_hi:[0,1,1]
	v_pk_fma_f32 v[58:59], v[134:135], v[142:143], v[58:59] op_sel_hi:[0,1,1]
	v_pk_fma_f32 v[56:57], v[134:135], v[140:141], v[56:57] op_sel_hi:[0,1,1]
	v_mfma_f32_32x32x16_bf16 v[4:19], v[24:27], v[152:155], v[4:19]
	ds_read_b128 v[152:155], v170 offset:864
	v_fma_f32 v54, v134, v138, v54
	v_fma_f32 v55, v134, v139, v55
	s_waitcnt lgkmcnt(3)
	v_mfma_f32_32x32x16_bf16 v[4:19], v[28:31], v[252:255], v[4:19]
	s_waitcnt lgkmcnt(0)
	v_mfma_f32_32x32x16_bf16 v[4:19], v[32:35], v[152:155], v[4:19]
	s_nop 11
	v_max_f32_e32 v166, 0, v4
	v_max_f32_e32 v167, 0, v5
	v_max_f32_e32 v164, 0, v6
	v_max_f32_e32 v165, 0, v7
	v_max_f32_e32 v162, 0, v8
	v_max_f32_e32 v163, 0, v9
	v_max_f32_e32 v160, 0, v10
	v_max_f32_e32 v161, 0, v11
	v_max_f32_e32 v158, 0, v12
	v_max_f32_e32 v159, 0, v13
	v_max_f32_e32 v156, 0, v14
	v_max_f32_e32 v157, 0, v15
	v_max_f32_e32 v154, 0, v16
	v_max_f32_e32 v155, 0, v17
	v_max_f32_e32 v152, 0, v18
	v_max_f32_e32 v153, 0, v19
	s_waitcnt lgkmcnt(0)
	v_mfma_f32_32x32x16_bf16 v[4:19], v[20:23], v[240:243], 0
	v_fma_f32 v66, v38, v166, v66
	v_fma_f32 v67, v38, v167, v67
	v_fma_f32 v64, v38, v164, v64
	v_fma_f32 v65, v38, v165, v65
	v_fma_f32 v36, v38, v152, v36
	v_fma_f32 v37, v38, v153, v37
	v_pk_fma_f32 v[62:63], v[38:39], v[162:163], v[62:63] op_sel_hi:[0,1,1]
	v_pk_fma_f32 v[60:61], v[38:39], v[160:161], v[60:61] op_sel_hi:[0,1,1]
	v_pk_fma_f32 v[58:59], v[38:39], v[158:159], v[58:59] op_sel_hi:[0,1,1]
	v_pk_fma_f32 v[56:57], v[38:39], v[156:157], v[56:57] op_sel_hi:[0,1,1]
	v_mfma_f32_32x32x16_bf16 v[4:19], v[24:27], v[172:175], v[4:19]
	ds_read_b128 v[172:175], v170 offset:992
	v_fma_f32 v54, v38, v154, v54
	v_fma_f32 v55, v38, v155, v55
	s_waitcnt lgkmcnt(1)
	v_mfma_f32_32x32x16_bf16 v[4:19], v[28:31], v[248:251], v[4:19]
	s_waitcnt lgkmcnt(0)
	v_mfma_f32_32x32x16_bf16 v[4:19], v[32:35], v[172:175], v[4:19]
	v_mul_f32_e32 v170, 0x3d3504f3, v39
	s_nop 10
	v_max_f32_e32 v4, 0, v4
	v_max_f32_e32 v5, 0, v5
	v_max_f32_e32 v6, 0, v6
	v_max_f32_e32 v7, 0, v7
	v_max_f32_e32 v18, 0, v18
	v_max_f32_e32 v19, 0, v19
	v_pk_fma_f32 v[4:5], v[170:171], v[4:5], v[66:67] op_sel_hi:[0,1,1]
	v_pk_fma_f32 v[6:7], v[170:171], v[6:7], v[64:65] op_sel_hi:[0,1,1]
	v_max_f32_e32 v8, 0, v8
	v_max_f32_e32 v9, 0, v9
	v_max_f32_e32 v10, 0, v10
	v_max_f32_e32 v11, 0, v11
	v_max_f32_e32 v12, 0, v12
	v_max_f32_e32 v13, 0, v13
	v_max_f32_e32 v14, 0, v14
	v_max_f32_e32 v15, 0, v15
	v_max_f32_e32 v16, 0, v16
	v_max_f32_e32 v17, 0, v17
	v_pk_fma_f32 v[18:19], v[170:171], v[18:19], v[36:37] op_sel_hi:[0,1,1]
	v_lshl_add_u64 v[36:37], v[2:3], 2, v[50:51]
	v_pk_fma_f32 v[8:9], v[170:171], v[8:9], v[62:63] op_sel_hi:[0,1,1]
	v_pk_fma_f32 v[10:11], v[170:171], v[10:11], v[60:61] op_sel_hi:[0,1,1]
	v_pk_fma_f32 v[12:13], v[170:171], v[12:13], v[58:59] op_sel_hi:[0,1,1]
	v_pk_fma_f32 v[14:15], v[170:171], v[14:15], v[56:57] op_sel_hi:[0,1,1]
	v_pk_fma_f32 v[16:17], v[170:171], v[16:17], v[54:55] op_sel_hi:[0,1,1]
	global_store_dwordx4 v[36:37], v[4:7], off
	global_store_dwordx4 v[36:37], v[8:11], off offset:32
	global_store_dwordx4 v[36:37], v[12:15], off offset:64
	global_store_dwordx4 v[36:37], v[16:19], off offset:96
	s_cbranch_vccz .LBB0_409
	s_add_i32 s7, s7, 8
	s_cmp_ge_i32 s7, s6
	s_cbranch_scc0 .LBB0_408
